# speedup vs baseline: 1.0105x; 1.0105x over previous
.Lk_220:
	s_lshr_b32 s0, s14, 6
	s_mul_i32 s1, s0, 0x1c2
	s_add_u32 s1, s1, s33
	v_and_b32_e32 v1, 63, v0
	v_and_b32_e32 v2, 1, v0
	v_add_u32_e32 v2, 64, v2
	v_add_u32_e32 v3, s1, v1
	v_add_u32_e32 v4, s1, v2
	v_lshlrev_b32_e32 v5, 4, v3
	v_lshlrev_b32_e32 v3, 2, v3
	v_lshlrev_b32_e32 v6, 4, v4
	v_lshlrev_b32_e32 v4, 2, v4
	global_load_dwordx4 v[8:11], v5, s[54:55]
	global_load_dword v16, v3, s[56:57]
	global_load_dwordx4 v[12:15], v6, s[54:55]
	global_load_dword v17, v4, s[56:57]
	s_lshl_b32 s0, s0, 2
	v_lshlrev_b32_e32 v18, 6, v1
	v_add_u32_e32 v18, s0, v18
	v_lshlrev_b32_e32 v19, 2, v18
	v_add_u32_e32 v18, 0x1c200, v18
	v_lshlrev_b32_e32 v20, 6, v2
	v_add_u32_e32 v20, s0, v20
	v_lshlrev_b32_e32 v21, 2, v20
	v_add_u32_e32 v20, 0x1c200, v20
	s_waitcnt vmcnt(2)
	v_cvt_pk_f16_f32 v22, v8, v9
	v_cvt_pk_f16_f32 v23, v10, v11
	v_cvt_f16_f32_e32 v26, v16
	v_cvt_f32_f16_e32 v28, v22
	v_cvt_f32_f16_sdwa v29, v22 dst_sel:DWORD dst_unused:UNUSED_PAD src0_sel:WORD_1
	v_cvt_f32_f16_e32 v30, v23
	v_cvt_f32_f16_sdwa v31, v23 dst_sel:DWORD dst_unused:UNUSED_PAD src0_sel:WORD_1
	v_cvt_f32_f16_e32 v26, v26
	v_pk_add_f32 v[28:29], v[8:9], v[28:29] neg_lo:[0,1] neg_hi:[0,1]
	v_pk_add_f32 v[30:31], v[10:11], v[30:31] neg_lo:[0,1] neg_hi:[0,1]
	v_sub_f32_e32 v26, v16, v26
	v_cvt_pk_f16_f32 v24, v28, v29
	v_cvt_pk_f16_f32 v25, v30, v31
	v_cvt_pk_f16_f32 v26, v16, v26
	ds_write_b128 v19, v[22:25]
	ds_write_b32 v18, v26
	s_waitcnt vmcnt(0)
	v_cvt_pk_f16_f32 v22, v12, v13
	v_cvt_pk_f16_f32 v23, v14, v15
	v_cvt_f16_f32_e32 v26, v17
	v_cvt_f32_f16_e32 v28, v22
	v_cvt_f32_f16_sdwa v29, v22 dst_sel:DWORD dst_unused:UNUSED_PAD src0_sel:WORD_1
	v_cvt_f32_f16_e32 v30, v23
	v_cvt_f32_f16_sdwa v31, v23 dst_sel:DWORD dst_unused:UNUSED_PAD src0_sel:WORD_1
	v_cvt_f32_f16_e32 v26, v26
	v_pk_add_f32 v[28:29], v[12:13], v[28:29] neg_lo:[0,1] neg_hi:[0,1]
	v_pk_add_f32 v[30:31], v[14:15], v[30:31] neg_lo:[0,1] neg_hi:[0,1]
	v_sub_f32_e32 v26, v17, v26
	v_cvt_pk_f16_f32 v24, v28, v29
	v_cvt_pk_f16_f32 v25, v30, v31
	v_cvt_pk_f16_f32 v26, v17, v26
	ds_write_b128 v21, v[22:25]
	ds_write_b32 v20, v26
	s_mov_b64 s[0:1], exec

.Lk_298:
	s_and_b64 vcc, exec, s[0:1]
	s_cbranch_vccz .Lk_313
	s_setprio 2
	s_mul_i32 s68, s15, 0x1c2
	s_add_u32 s68, s68, s33
	s_add_u32 s68, s68, 66
	s_lshl_b32 s69, s68, 4
	s_add_u32 s70, s54, s69
	s_addc_u32 s71, s55, 0
	s_add_u32 s72, s70, 0xe100
	s_addc_u32 s73, s71, 0
	s_lshl_b32 s69, s68, 2
	s_add_u32 s74, s56, s69
	s_addc_u32 s75, s57, 0
	s_add_u32 s76, s74, 0x3840
	s_addc_u32 s77, s75, 0
	v_lshlrev_b32_e32 v60, 4, v80
	v_lshlrev_b32_e32 v61, 2, v80
	global_load_dwordx4 v[64:67], v60, s[70:71]
	global_load_dwordx4 v[68:71], v60, s[72:73]
	global_load_dword v72, v61, s[74:75]
	global_load_dword v73, v61, s[76:77]
	s_lshl_b32 s69, s15, 2
	v_lshlrev_b32_e32 v63, 6, v80
	v_add_u32_e32 v63, s69, v63
	v_add_u32_e32 v63, 0x1080, v63
	v_lshlrev_b32_e32 v62, 2, v63
	v_add_u32_e32 v63, 0x1c200, v63
	ds_read_b128 v[34:37], v81
	v_mov_b32_e32 v40, 0
	v_mov_b32_e32 v41, 0
	s_mov_b32 s0, 0x4038aa3b
	s_mov_b32 s1, 0
	v_mov_b32_e32 v58, 0xc038aa3b
	v_mov_b32_e32 v59, 0xc038aa3b
	v_mov_b32_e32 v39, v81
	s_mov_b32 s9, 2
	s_waitcnt lgkmcnt(0)
	ds_read_b128 v[42:45], v78 offset:2048
	ds_read_b128 v[46:49], v78 offset:3072
	v_mfma_f32_16x16x32_f16 v[50:53], v[2:5], v[34:37], v[6:9]
	v_mfma_f32_16x16x32_f16 v[54:57], v[26:29], v[34:37], v[30:33]
	s_waitcnt lgkmcnt(1)
	v_mfma_f32_16x16x32_f16 v[50:53], v[18:21], v[42:45], v[50:53]
	v_mfma_f32_16x16x32_f16 v[54:57], v[10:13], v[42:45], v[54:57]
	s_waitcnt lgkmcnt(0)
	v_mfma_f32_16x16x32_f16 v[50:53], v[22:25], v[46:49], v[50:53]
	v_mfma_f32_16x16x32_f16 v[54:57], v[14:17], v[46:49], v[54:57]
	ds_read_b128 v[34:37], v39 offset:256
	s_nop 6
	v_exp_f32_e32 v84, v52
	v_exp_f32_e32 v85, v56
	v_exp_f32_e32 v86, v50
	v_exp_f32_e32 v87, v54
	v_exp_f32_e32 v88, v51
	v_exp_f32_e32 v89, v55
	v_pk_add_f32 v[90:91], v[84:85], 1.0 op_sel_hi:[1,0]
	v_pk_fma_f32 v[92:93], v[84:85], s[0:1], v[58:59] op_sel_hi:[1,0,0]
	v_pk_fma_f32 v[90:91], v[86:87], v[90:91], v[90:91]
	v_pk_fma_f32 v[94:95], v[90:91], v[88:89], v[90:91]
	v_rcp_f32_e32 v94, v94
	v_rcp_f32_e32 v95, v95
	v_pk_fma_f32 v[92:93], v[92:93], v[88:89], v[92:93]
	v_pk_fma_f32 v[92:93], v[40:41], v[90:91], v[92:93]
	v_exp_f32_e32 v96, v53
	v_pk_mul_f32 v[40:41], v[92:93], v[94:95]
	v_exp_f32_e32 v98, v40
	v_exp_f32_e32 v99, v41
	v_exp_f32_e32 v97, v57
	v_pk_add_f32 v[100:101], v[98:99], 1.0 op_sel_hi:[1,0]
	v_pk_fma_f32 v[100:101], v[100:101], v[96:97], v[100:101]
	v_rcp_f32_e32 v100, v100
	v_rcp_f32_e32 v101, v101
	v_pk_add_f32 v[102:103], v[98:99], -1.0 op_sel_hi:[1,0]
	v_pk_mul_f32 v[102:103], v[102:103], v[100:101]
	v_cvt_pk_f16_f32 v104, v102, v103
	ds_write_b32 v79, v104 offset:0
	s_waitcnt lgkmcnt(0)
	s_barrier
	ds_read_b128 v[42:45], v78 offset:0
	ds_read_b128 v[46:49], v78 offset:1024
	v_mfma_f32_16x16x32_f16 v[50:53], v[2:5], v[34:37], v[6:9]
	v_mfma_f32_16x16x32_f16 v[54:57], v[26:29], v[34:37], v[30:33]
	s_waitcnt lgkmcnt(1)
	v_mfma_f32_16x16x32_f16 v[50:53], v[18:21], v[42:45], v[50:53]
	v_mfma_f32_16x16x32_f16 v[54:57], v[10:13], v[42:45], v[54:57]
	s_waitcnt lgkmcnt(0)
	v_mfma_f32_16x16x32_f16 v[50:53], v[22:25], v[46:49], v[50:53]
	v_mfma_f32_16x16x32_f16 v[54:57], v[14:17], v[46:49], v[54:57]
	ds_read_b128 v[34:37], v39 offset:512
	s_nop 6
	v_exp_f32_e32 v84, v52
	v_exp_f32_e32 v85, v56
	v_exp_f32_e32 v86, v50
	v_exp_f32_e32 v87, v54
	v_exp_f32_e32 v88, v51
	v_exp_f32_e32 v89, v55
	v_pk_add_f32 v[90:91], v[84:85], 1.0 op_sel_hi:[1,0]
	v_pk_fma_f32 v[92:93], v[84:85], s[0:1], v[58:59] op_sel_hi:[1,0,0]
	v_pk_fma_f32 v[90:91], v[86:87], v[90:91], v[90:91]
	v_pk_fma_f32 v[94:95], v[90:91], v[88:89], v[90:91]
	v_rcp_f32_e32 v94, v94
	v_rcp_f32_e32 v95, v95
	v_pk_fma_f32 v[92:93], v[92:93], v[88:89], v[92:93]
	v_pk_fma_f32 v[92:93], v[40:41], v[90:91], v[92:93]
	v_exp_f32_e32 v96, v53
	v_pk_mul_f32 v[40:41], v[92:93], v[94:95]
	v_exp_f32_e32 v98, v40
	v_exp_f32_e32 v99, v41
	v_exp_f32_e32 v97, v57
	v_pk_add_f32 v[100:101], v[98:99], 1.0 op_sel_hi:[1,0]
	v_pk_fma_f32 v[100:101], v[100:101], v[96:97], v[100:101]
	v_rcp_f32_e32 v100, v100
	v_rcp_f32_e32 v101, v101
	v_pk_add_f32 v[102:103], v[98:99], -1.0 op_sel_hi:[1,0]
	v_pk_mul_f32 v[102:103], v[102:103], v[100:101]
	v_cvt_pk_f16_f32 v104, v102, v103
	ds_write_b32 v79, v104 offset:2048
	s_waitcnt lgkmcnt(0)
	v_add_u32_e32 v39, 0x200, v39
	.p2align	6
.Lpa_loop:
	s_barrier
	ds_read_b128 v[42:45], v78 offset:2048
	ds_read_b128 v[46:49], v78 offset:3072
	v_mfma_f32_16x16x32_f16 v[50:53], v[2:5], v[34:37], v[6:9]
	v_mfma_f32_16x16x32_f16 v[54:57], v[26:29], v[34:37], v[30:33]
	s_waitcnt lgkmcnt(1)
	v_mfma_f32_16x16x32_f16 v[50:53], v[18:21], v[42:45], v[50:53]
	v_mfma_f32_16x16x32_f16 v[54:57], v[10:13], v[42:45], v[54:57]
	s_waitcnt lgkmcnt(0)
	v_mfma_f32_16x16x32_f16 v[50:53], v[22:25], v[46:49], v[50:53]
	v_mfma_f32_16x16x32_f16 v[54:57], v[14:17], v[46:49], v[54:57]
	ds_read_b128 v[34:37], v39 offset:256
	s_nop 6
	v_min_f32_e32 v40, 0x42700000, v40
	v_min_f32_e32 v41, 0x42700000, v41
	v_exp_f32_e32 v84, v52
	v_exp_f32_e32 v85, v56
	v_exp_f32_e32 v86, v50
	v_exp_f32_e32 v87, v54
	v_exp_f32_e32 v88, v51
	v_exp_f32_e32 v89, v55
	v_pk_add_f32 v[90:91], v[84:85], 1.0 op_sel_hi:[1,0]
	v_pk_fma_f32 v[92:93], v[84:85], s[0:1], v[58:59] op_sel_hi:[1,0,0]
	v_pk_fma_f32 v[90:91], v[86:87], v[90:91], v[90:91]
	v_pk_fma_f32 v[94:95], v[90:91], v[88:89], v[90:91]
	v_rcp_f32_e32 v94, v94
	v_rcp_f32_e32 v95, v95
	v_pk_fma_f32 v[92:93], v[92:93], v[88:89], v[92:93]
	v_pk_fma_f32 v[92:93], v[40:41], v[90:91], v[92:93]
	v_exp_f32_e32 v96, v53
	v_pk_mul_f32 v[40:41], v[92:93], v[94:95]
	v_exp_f32_e32 v98, v40
	v_exp_f32_e32 v99, v41
	v_exp_f32_e32 v97, v57
	v_pk_add_f32 v[100:101], v[98:99], 1.0 op_sel_hi:[1,0]
	v_pk_fma_f32 v[100:101], v[100:101], v[96:97], v[100:101]
	v_rcp_f32_e32 v100, v100
	v_rcp_f32_e32 v101, v101
	v_pk_add_f32 v[102:103], v[98:99], -1.0 op_sel_hi:[1,0]
	v_pk_mul_f32 v[102:103], v[102:103], v[100:101]
	v_cvt_pk_f16_f32 v104, v102, v103
	ds_write_b32 v79, v104 offset:0
	s_waitcnt lgkmcnt(0)
	s_barrier
	ds_read_b128 v[42:45], v78 offset:0
	ds_read_b128 v[46:49], v78 offset:1024
	v_mfma_f32_16x16x32_f16 v[50:53], v[2:5], v[34:37], v[6:9]
	v_mfma_f32_16x16x32_f16 v[54:57], v[26:29], v[34:37], v[30:33]
	s_waitcnt lgkmcnt(1)
	v_mfma_f32_16x16x32_f16 v[50:53], v[18:21], v[42:45], v[50:53]
	v_mfma_f32_16x16x32_f16 v[54:57], v[10:13], v[42:45], v[54:57]
	s_waitcnt lgkmcnt(0)
	v_mfma_f32_16x16x32_f16 v[50:53], v[22:25], v[46:49], v[50:53]
	v_mfma_f32_16x16x32_f16 v[54:57], v[14:17], v[46:49], v[54:57]
	ds_read_b128 v[34:37], v39 offset:512
	s_nop 6
	v_exp_f32_e32 v84, v52
	v_exp_f32_e32 v85, v56
	v_exp_f32_e32 v86, v50
	v_exp_f32_e32 v87, v54
	v_exp_f32_e32 v88, v51
	v_exp_f32_e32 v89, v55
	v_pk_add_f32 v[90:91], v[84:85], 1.0 op_sel_hi:[1,0]
	v_pk_fma_f32 v[92:93], v[84:85], s[0:1], v[58:59] op_sel_hi:[1,0,0]
	v_pk_fma_f32 v[90:91], v[86:87], v[90:91], v[90:91]
	v_pk_fma_f32 v[94:95], v[90:91], v[88:89], v[90:91]
	v_rcp_f32_e32 v94, v94
	v_rcp_f32_e32 v95, v95
	v_pk_fma_f32 v[92:93], v[92:93], v[88:89], v[92:93]
	v_pk_fma_f32 v[92:93], v[40:41], v[90:91], v[92:93]
	v_exp_f32_e32 v96, v53
	v_pk_mul_f32 v[40:41], v[92:93], v[94:95]
	v_exp_f32_e32 v98, v40
	v_exp_f32_e32 v99, v41
	v_exp_f32_e32 v97, v57
	v_pk_add_f32 v[100:101], v[98:99], 1.0 op_sel_hi:[1,0]
	v_pk_fma_f32 v[100:101], v[100:101], v[96:97], v[100:101]
	v_rcp_f32_e32 v100, v100
	v_rcp_f32_e32 v101, v101
	v_pk_add_f32 v[102:103], v[98:99], -1.0 op_sel_hi:[1,0]
	v_pk_mul_f32 v[102:103], v[102:103], v[100:101]
	v_cvt_pk_f16_f32 v104, v102, v103
	ds_write_b32 v79, v104 offset:2048
	s_waitcnt lgkmcnt(0)
	s_barrier
	ds_read_b128 v[42:45], v78 offset:2048
	ds_read_b128 v[46:49], v78 offset:3072
	v_mfma_f32_16x16x32_f16 v[50:53], v[2:5], v[34:37], v[6:9]
	v_mfma_f32_16x16x32_f16 v[54:57], v[26:29], v[34:37], v[30:33]
	s_waitcnt lgkmcnt(1)
	v_mfma_f32_16x16x32_f16 v[50:53], v[18:21], v[42:45], v[50:53]
	v_mfma_f32_16x16x32_f16 v[54:57], v[10:13], v[42:45], v[54:57]
	s_waitcnt lgkmcnt(0)
	v_mfma_f32_16x16x32_f16 v[50:53], v[22:25], v[46:49], v[50:53]
	v_mfma_f32_16x16x32_f16 v[54:57], v[14:17], v[46:49], v[54:57]
	ds_read_b128 v[34:37], v39 offset:768
	s_nop 6
	v_exp_f32_e32 v84, v52
	v_exp_f32_e32 v85, v56
	v_exp_f32_e32 v86, v50
	v_exp_f32_e32 v87, v54
	v_exp_f32_e32 v88, v51
	v_exp_f32_e32 v89, v55
	v_pk_add_f32 v[90:91], v[84:85], 1.0 op_sel_hi:[1,0]
	v_pk_fma_f32 v[92:93], v[84:85], s[0:1], v[58:59] op_sel_hi:[1,0,0]
	v_pk_fma_f32 v[90:91], v[86:87], v[90:91], v[90:91]
	v_pk_fma_f32 v[94:95], v[90:91], v[88:89], v[90:91]
	v_rcp_f32_e32 v94, v94
	v_rcp_f32_e32 v95, v95
	v_pk_fma_f32 v[92:93], v[92:93], v[88:89], v[92:93]
	v_pk_fma_f32 v[92:93], v[40:41], v[90:91], v[92:93]
	v_exp_f32_e32 v96, v53
	v_pk_mul_f32 v[40:41], v[92:93], v[94:95]
	v_exp_f32_e32 v98, v40
	v_exp_f32_e32 v99, v41
	v_exp_f32_e32 v97, v57
	v_pk_add_f32 v[100:101], v[98:99], 1.0 op_sel_hi:[1,0]
	v_pk_fma_f32 v[100:101], v[100:101], v[96:97], v[100:101]
	v_rcp_f32_e32 v100, v100
	v_rcp_f32_e32 v101, v101
	v_pk_add_f32 v[102:103], v[98:99], -1.0 op_sel_hi:[1,0]
	v_pk_mul_f32 v[102:103], v[102:103], v[100:101]
	v_cvt_pk_f16_f32 v104, v102, v103
	ds_write_b32 v79, v104 offset:0
	s_waitcnt lgkmcnt(0)
	s_barrier
	ds_read_b128 v[42:45], v78 offset:0
	ds_read_b128 v[46:49], v78 offset:1024
	v_mfma_f32_16x16x32_f16 v[50:53], v[2:5], v[34:37], v[6:9]
	v_mfma_f32_16x16x32_f16 v[54:57], v[26:29], v[34:37], v[30:33]
	s_waitcnt lgkmcnt(1)
	v_mfma_f32_16x16x32_f16 v[50:53], v[18:21], v[42:45], v[50:53]
	v_mfma_f32_16x16x32_f16 v[54:57], v[10:13], v[42:45], v[54:57]
	s_waitcnt lgkmcnt(0)
	v_mfma_f32_16x16x32_f16 v[50:53], v[22:25], v[46:49], v[50:53]
	v_mfma_f32_16x16x32_f16 v[54:57], v[14:17], v[46:49], v[54:57]
	ds_read_b128 v[34:37], v39 offset:1024
	s_nop 6
	v_exp_f32_e32 v84, v52
	v_exp_f32_e32 v85, v56
	v_exp_f32_e32 v86, v50
	v_exp_f32_e32 v87, v54
	v_exp_f32_e32 v88, v51
	v_exp_f32_e32 v89, v55
	v_pk_add_f32 v[90:91], v[84:85], 1.0 op_sel_hi:[1,0]
	v_pk_fma_f32 v[92:93], v[84:85], s[0:1], v[58:59] op_sel_hi:[1,0,0]
	v_pk_fma_f32 v[90:91], v[86:87], v[90:91], v[90:91]
	v_pk_fma_f32 v[94:95], v[90:91], v[88:89], v[90:91]
	v_rcp_f32_e32 v94, v94
	v_rcp_f32_e32 v95, v95
	v_pk_fma_f32 v[92:93], v[92:93], v[88:89], v[92:93]
	v_pk_fma_f32 v[92:93], v[40:41], v[90:91], v[92:93]
	v_exp_f32_e32 v96, v53
	v_pk_mul_f32 v[40:41], v[92:93], v[94:95]
	v_exp_f32_e32 v98, v40
	v_exp_f32_e32 v99, v41
	v_exp_f32_e32 v97, v57
	v_pk_add_f32 v[100:101], v[98:99], 1.0 op_sel_hi:[1,0]
	v_pk_fma_f32 v[100:101], v[100:101], v[96:97], v[100:101]
	v_rcp_f32_e32 v100, v100
	v_rcp_f32_e32 v101, v101
	v_pk_add_f32 v[102:103], v[98:99], -1.0 op_sel_hi:[1,0]
	v_pk_mul_f32 v[102:103], v[102:103], v[100:101]
	v_cvt_pk_f16_f32 v104, v102, v103
	ds_write_b32 v79, v104 offset:2048
	s_waitcnt lgkmcnt(0)
	s_add_u32 s9, s9, 4
	v_add_u32_e32 v39, 0x400, v39
	s_bitcmp0_b32 s9, 2
	s_cbranch_scc1 .Lpa_stream
.Lpa_stream_ret:
	s_cmp_lt_u32 s9, 450
	s_cbranch_scc1 .Lpa_loop
	s_barrier
	s_endpgm
.Lpa_stream:
	s_cmp_gt_u32 s9, 50
	s_cbranch_scc1 .Lpa_stream_ret
	s_waitcnt vmcnt(0)
	v_cvt_pk_f16_f32 v74, v64, v65
	v_cvt_pk_f16_f32 v75, v66, v67
	v_cvt_f16_f32_e32 v112, v72
	v_cvt_f32_f16_e32 v108, v74
	v_cvt_f32_f16_sdwa v109, v74 dst_sel:DWORD dst_unused:UNUSED_PAD src0_sel:WORD_1
	v_cvt_f32_f16_e32 v110, v75
	v_cvt_f32_f16_sdwa v111, v75 dst_sel:DWORD dst_unused:UNUSED_PAD src0_sel:WORD_1
	v_cvt_f32_f16_e32 v112, v112
	v_pk_add_f32 v[108:109], v[64:65], v[108:109] neg_lo:[0,1] neg_hi:[0,1]
	v_pk_add_f32 v[110:111], v[66:67], v[110:111] neg_lo:[0,1] neg_hi:[0,1]
	v_sub_f32_e32 v112, v72, v112
	v_cvt_pk_f16_f32 v76, v108, v109
	v_cvt_pk_f16_f32 v77, v110, v111
	v_cvt_pk_f16_f32 v112, v72, v112
	ds_write_b128 v62, v[74:77]
	ds_write_b32 v63, v112
	v_cvt_pk_f16_f32 v74, v68, v69
	v_cvt_pk_f16_f32 v75, v70, v71
	v_cvt_f16_f32_e32 v112, v73
	v_cvt_f32_f16_e32 v108, v74
	v_cvt_f32_f16_sdwa v109, v74 dst_sel:DWORD dst_unused:UNUSED_PAD src0_sel:WORD_1
	v_cvt_f32_f16_e32 v110, v75
	v_cvt_f32_f16_sdwa v111, v75 dst_sel:DWORD dst_unused:UNUSED_PAD src0_sel:WORD_1
	v_cvt_f32_f16_e32 v112, v112
	v_pk_add_f32 v[108:109], v[68:69], v[108:109] neg_lo:[0,1] neg_hi:[0,1]
	v_pk_add_f32 v[110:111], v[70:71], v[110:111] neg_lo:[0,1] neg_hi:[0,1]
	v_sub_f32_e32 v112, v73, v112
	v_cvt_pk_f16_f32 v76, v108, v109
	v_cvt_pk_f16_f32 v77, v110, v111
	v_cvt_pk_f16_f32 v112, v73, v112
	ds_write_b128 v62, v[74:77] offset:128
	ds_write_b32 v63, v112 offset:32
	v_add_u32_e32 v62, 0x4000, v62
	v_add_u32_e32 v63, 0x1000, v63
	s_add_u32 s70, s70, 0x400
	s_addc_u32 s71, s71, 0
	s_add_u32 s72, s72, 0x400
	s_addc_u32 s73, s73, 0
	s_add_u32 s74, s74, 0x100
	s_addc_u32 s75, s75, 0
	s_add_u32 s76, s76, 0x100
	s_addc_u32 s77, s77, 0
	s_cmp_eq_u32 s9, 50
	s_cbranch_scc1 .Lpa_stream_ret
	global_load_dwordx4 v[64:67], v60, s[70:71]
	global_load_dwordx4 v[68:71], v60, s[72:73]
	global_load_dword v72, v61, s[74:75]
	global_load_dword v73, v61, s[76:77]
	s_branch .Lpa_stream_ret
